# P1 rope epilogue: (cos,sin) table copied to LDS at phase start, 32 table reads per unit via ds_read_b128 instead of global loads + vmcnt(0) drains
# baseline (speedup 1.0000x reference)
;     __host__ __device__ bool next(int i, Unit& u) const {
;         const long L = (long)i * G + c; if (L >= nwg) return false;
;         int wgid = (int)L; { const int q = nwg / NXCD, r = nwg % NXCD, xcd = wgid % NXCD, off = wgid / NXCD; wgid = (xcd < r ? xcd * (q + 1) : r * (q + 1) + (xcd - r) * q) + off; }
;         const int nig = WGM * nN, gid = wgid / nig, fm = gid * WGM, gsz = (nM - fm) < WGM ? (nM - fm) : WGM;
;         u.pm = fm + ((wgid % nig) % gsz); u.pn = (wgid % nig) / gsz; u.pb = u.pn; return true;
; __global__ void __launch_bounds__(NWAVES * 64, 2) enc_fwd(Args args) {
;     ...
;         const int Gg = (G == 256) ? G_P1 : G;
;         if (blk < Gg) {
;             pg8::Gemm g{XN, WIN0, NTOK, L0_IN, DM / 2}; pg8::StaticOrder S; S.init(NTOK, L0_IN, Gg, blk);
;             pg8::EpiHeads0 E{AQ, AK, AV, BQ, BK, BV, args.in[4], args.in[5], args.in[6], args.in[7], (const pg8::f32x2e*)ROPE, QSCALE, QSCALE * KAPPA};
;             pg8::gemm_phase<pg8::EpiHeads0, pg8::StaticOrder, PG8_ALIGN, PG8_SP2, true>(lds, g, S, E);
.LBB0_141:
	s_and_b64 vcc, exec, s[4:5]
	s_cbranch_vccz .LBB0_284
	v_lshlrev_b32_e32 v240, 5, v0
	s_sub_u32 s100, 0x20000, s16
	global_load_dwordx4 v[242:245], v240, s[16:17]
	global_load_dwordx4 v[246:249], v240, s[16:17] offset:16
	v_add_u32_e32 v241, 0x20000, v240
	s_waitcnt vmcnt(0)
	ds_write_b128 v241, v[242:245]
	ds_write_b128 v241, v[246:249] offset:16
	s_waitcnt lgkmcnt(0)
	v_readlane_b32 s0, v254, 10
	s_cmpk_lt_i32 s0, 0x480
	s_cselect_b64 s[2:3], -1, 0
	s_cmpk_gt_i32 s0, 0x47f
	v_readfirstlane_b32 s0, v0
	s_cbranch_scc1 .LBB0_144
	s_ashr_i32 s1, s35, 3
	s_cmp_lt_i32 s34, 0
	s_movk_i32 s4, 0x91
	s_cselect_b32 s4, s4, 0x90
	s_mul_i32 s4, s34, s4
	s_add_i32 s4, s4, s1
	s_mul_hi_i32 s1, s4, 0x38e38e39
	s_lshr_b32 s5, s1, 31
	s_ashr_i32 s1, s1, 4
	s_add_i32 s1, s1, s5
	s_lshl_b32 s5, s1, 3
	s_mulk_i32 s1, 0x48
	s_sub_i32 s1, s4, s1
	s_bfe_i32 s4, s1, 0x80000
	s_bfe_u32 s4, s4, 0x3000c
	s_add_i32 s4, s1, s4
	s_bfe_i32 s6, s4, 0x80000
	s_and_b32 s4, s4, 0xf8
	s_sub_i32 s1, s1, s4
	s_sext_i32_i16 s7, s6
	s_sext_i32_i8 s1, s1
	s_add_i32 s6, s5, s1
	s_ashr_i32 s4, s7, 3

; template <bool F8OUT = false> __device__ __forceinline__ void head_tile_store(const f32x4 (&acc)[2][2][4][2], bf16_t* obase  , int opitch, const float* gain, float scale, const f32x2e* rope, int row0, int fq) {
;     ...
;             if (rope) {
;                 const int t = row & 8191; const bool second = (fq & 2) != 0;
; #pragma unroll
;                 for (int bj = 0; bj < 2; ++bj) { const int pos = bj ? (t & 63) : (t >> 6); const f32x2e* tb = rope + pos * 16 + 8 * (fq & 1);
; #pragma unroll
;                     for (int n = 0; n < 2; ++n)
; #pragma unroll
;                         for (int e = 0; e < 4; ++e) { const float p = __shfl_xor(x[bj][n][e], 32); const f32x2e cs = tb[4 * n + e]; const float v = x[bj][n][e];
;                             x[bj][n][e] = second ? (p * cs.y + v * cs.x) : (v * cs.x - p * cs.y); } }
;             }
.LBB0_167:
	v_and_b32_e32 v162, 2, v162
	v_readlane_b32 s0, v255, 21
	v_cmp_eq_u32_e64 s[4:5], 0, v162
	v_and_b32_e32 v162, 8, v190
	v_readlane_b32 s1, v255, 22
	v_lshlrev_b32_e32 v174, 3, v162
	v_and_b32_e32 v185, 63, v188
	v_cndmask_b32_e64 v162, 0, 1, s[0:1]
	v_lshl_add_u64 v[186:187], s[16:17], 0, v[174:175]
	v_cmp_ne_u32_e64 s[8:9], 1, v162
	s_andn2_b64 vcc, exec, s[0:1]
	v_lshlrev_b32_e32 v198, 7, v185
	s_cbranch_vccnz .LBB0_169
	v_and_b32_e32 v163, 64, v212
	v_xor_b32_e32 v162, 32, v212
	v_add_u32_e32 v163, 64, v163
	v_cmp_lt_i32_e32 vcc, v162, v163
	v_mov_b32_e32 v199, v175
	s_nop 0
	v_cndmask_b32_e32 v162, v212, v162, vcc
	v_lshlrev_b32_e32 v189, 2, v162
	v_lshlrev_b32_e32 v162, 1, v188
	v_and_b32_e32 v174, 0x3f80, v162
	v_lshl_add_u64 v[196:197], v[186:187], 0, v[174:175]
	v_add_u32_e32 v238, s100, v196
	ds_read_b128 v[162:165], v238 offset:48
	ds_read_b128 v[192:195], v238 offset:32
	ds_read_b128 v[214:217], v238 offset:16
	ds_read_b128 v[218:221], v238
	ds_bpermute_b32 v200, v189, v18
	ds_bpermute_b32 v201, v189, v19
	s_waitcnt lgkmcnt(0)
	v_mov_b32_e32 v196, v219
	v_mov_b32_e32 v197, v221
	s_waitcnt lgkmcnt(0)
	v_pk_mul_f32 v[196:197], v[196:197], v[200:201]
	v_mov_b32_e32 v219, v220
	v_cndmask_b32_e64 v197, v197, -v197, s[4:5]
	v_cndmask_b32_e64 v196, v196, -v196, s[4:5]
	v_pk_fma_f32 v[18:19], v[18:19], v[218:219], v[196:197]
	ds_bpermute_b32 v196, v189, v20
	ds_bpermute_b32 v197, v189, v21
	v_mov_b32_e32 v200, v215
	v_mov_b32_e32 v201, v217
	v_mov_b32_e32 v215, v216
	s_waitcnt lgkmcnt(0)
	v_pk_mul_f32 v[196:197], v[200:201], v[196:197]
	s_nop 0
	v_cndmask_b32_e64 v197, v197, -v197, s[4:5]
	v_cndmask_b32_e64 v196, v196, -v196, s[4:5]
	v_pk_fma_f32 v[20:21], v[20:21], v[214:215], v[196:197]
	ds_bpermute_b32 v196, v189, v22
	ds_bpermute_b32 v197, v189, v23
	v_mov_b32_e32 v200, v193
	v_mov_b32_e32 v201, v195
	v_mov_b32_e32 v193, v194
	s_waitcnt lgkmcnt(0)
	v_pk_mul_f32 v[196:197], v[200:201], v[196:197]
	s_nop 0
	v_cndmask_b32_e64 v195, v197, -v197, s[4:5]
	v_cndmask_b32_e64 v194, v196, -v196, s[4:5]
	v_pk_fma_f32 v[22:23], v[22:23], v[192:193], v[194:195]
	ds_bpermute_b32 v192, v189, v24
	ds_bpermute_b32 v193, v189, v25
	v_mov_b32_e32 v194, v163
	v_mov_b32_e32 v195, v165
	v_mov_b32_e32 v163, v164
	v_lshl_add_u64 v[196:197], v[186:187], 0, v[198:199]
	s_waitcnt lgkmcnt(0)
	v_pk_mul_f32 v[192:193], v[194:195], v[192:193]
	ds_bpermute_b32 v200, v189, v26
	v_cndmask_b32_e64 v165, v193, -v193, s[4:5]
	v_cndmask_b32_e64 v164, v192, -v192, s[4:5]
	v_pk_fma_f32 v[24:25], v[24:25], v[162:163], v[164:165]
	v_add_u32_e32 v238, s100, v196
	ds_read_b128 v[162:165], v238 offset:48
	ds_read_b128 v[192:195], v238 offset:32
	ds_read_b128 v[214:217], v238 offset:16
	ds_read_b128 v[218:221], v238
	ds_bpermute_b32 v201, v189, v27
	s_waitcnt lgkmcnt(0)
	v_mov_b32_e32 v196, v219
	v_mov_b32_e32 v197, v221
	s_waitcnt lgkmcnt(0)
	v_pk_mul_f32 v[196:197], v[196:197], v[200:201]
	v_mov_b32_e32 v219, v220
	v_cndmask_b32_e64 v197, v197, -v197, s[4:5]
	v_cndmask_b32_e64 v196, v196, -v196, s[4:5]
	v_pk_fma_f32 v[26:27], v[26:27], v[218:219], v[196:197]
	ds_bpermute_b32 v196, v189, v28
	ds_bpermute_b32 v197, v189, v29
	v_mov_b32_e32 v200, v215
	v_mov_b32_e32 v201, v217
	v_mov_b32_e32 v215, v216
	s_waitcnt lgkmcnt(0)
	v_pk_mul_f32 v[196:197], v[200:201], v[196:197]
	s_nop 0
	v_cndmask_b32_e64 v197, v197, -v197, s[4:5]
	v_cndmask_b32_e64 v196, v196, -v196, s[4:5]
	v_pk_fma_f32 v[28:29], v[28:29], v[214:215], v[196:197]
	ds_bpermute_b32 v196, v189, v30
	ds_bpermute_b32 v197, v189, v31
	v_mov_b32_e32 v200, v193
	v_mov_b32_e32 v201, v195
	v_mov_b32_e32 v193, v194
	s_waitcnt lgkmcnt(0)
	v_pk_mul_f32 v[196:197], v[200:201], v[196:197]
	s_nop 0
	v_cndmask_b32_e64 v195, v197, -v197, s[4:5]
	v_cndmask_b32_e64 v194, v196, -v196, s[4:5]
	v_pk_fma_f32 v[30:31], v[30:31], v[192:193], v[194:195]
	ds_bpermute_b32 v192, v189, v32
	ds_bpermute_b32 v193, v189, v33
	v_mov_b32_e32 v194, v163
	v_mov_b32_e32 v195, v165
	v_mov_b32_e32 v163, v164
	s_waitcnt lgkmcnt(0)
	v_pk_mul_f32 v[192:193], v[194:195], v[192:193]
	s_nop 0
	v_cndmask_b32_e64 v165, v193, -v193, s[4:5]
	v_cndmask_b32_e64 v164, v192, -v192, s[4:5]
	v_pk_fma_f32 v[32:33], v[32:33], v[162:163], v[164:165]

; template <bool F8OUT = false> __device__ __forceinline__ void head_tile_store(const f32x4 (&acc)[2][2][4][2], bf16_t* obase  , int opitch, const float* gain, float scale, const f32x2e* rope, int row0, int fq) {
;     ...
;             if (rope) {
;                 const int t = row & 8191; const bool second = (fq & 2) != 0;
; #pragma unroll
;                 for (int bj = 0; bj < 2; ++bj) { const int pos = bj ? (t & 63) : (t >> 6); const f32x2e* tb = rope + pos * 16 + 8 * (fq & 1);
; #pragma unroll
;                     for (int n = 0; n < 2; ++n)
; #pragma unroll
;                         for (int e = 0; e < 4; ++e) { const float p = __shfl_xor(x[bj][n][e], 32); const f32x2e cs = tb[4 * n + e]; const float v = x[bj][n][e];
;                             x[bj][n][e] = second ? (p * cs.y + v * cs.x) : (v * cs.x - p * cs.y); } }
;             }
.LBB0_171:
	v_add_u32_e32 v194, 16, v188
	v_and_b32_e32 v162, 63, v194
	s_and_b64 vcc, exec, s[8:9]
	v_lshlrev_b32_e32 v192, 7, v162
	s_cbranch_vccnz .LBB0_173
	v_and_b32_e32 v163, 64, v212
	v_xor_b32_e32 v162, 32, v212
	v_add_u32_e32 v163, 64, v163
	v_cmp_lt_i32_e32 vcc, v162, v163
	v_mov_b32_e32 v193, v175
	s_nop 0
	v_cndmask_b32_e32 v162, v212, v162, vcc
	v_lshlrev_b32_e32 v189, 2, v162
	v_lshlrev_b32_e32 v162, 1, v194
	v_and_b32_e32 v174, 0x3f80, v162
	v_lshl_add_u64 v[196:197], v[186:187], 0, v[174:175]
	v_add_u32_e32 v238, s100, v196
	ds_read_b128 v[162:165], v238 offset:48
	ds_read_b128 v[214:217], v238 offset:32
	ds_read_b128 v[218:221], v238 offset:16
	ds_read_b128 v[222:225], v238
	ds_bpermute_b32 v200, v189, v26
	ds_bpermute_b32 v201, v189, v27
	s_waitcnt lgkmcnt(0)
	v_mov_b32_e32 v196, v223
	v_mov_b32_e32 v197, v225
	s_waitcnt lgkmcnt(0)
	v_pk_mul_f32 v[196:197], v[196:197], v[200:201]
	v_mov_b32_e32 v223, v224
	v_cndmask_b32_e64 v197, v197, -v197, s[4:5]
	v_cndmask_b32_e64 v196, v196, -v196, s[4:5]
	v_pk_fma_f32 v[26:27], v[26:27], v[222:223], v[196:197]
	ds_bpermute_b32 v196, v189, v28
	ds_bpermute_b32 v197, v189, v29
	v_mov_b32_e32 v200, v219
	v_mov_b32_e32 v201, v221
	v_mov_b32_e32 v219, v220
	s_waitcnt lgkmcnt(0)
	v_pk_mul_f32 v[196:197], v[200:201], v[196:197]
	s_nop 0
	v_cndmask_b32_e64 v197, v197, -v197, s[4:5]
	v_cndmask_b32_e64 v196, v196, -v196, s[4:5]
	v_pk_fma_f32 v[28:29], v[28:29], v[218:219], v[196:197]
	ds_bpermute_b32 v196, v189, v30
	ds_bpermute_b32 v197, v189, v31
	v_mov_b32_e32 v200, v215
	v_mov_b32_e32 v201, v217
	v_mov_b32_e32 v215, v216
	s_waitcnt lgkmcnt(0)
	v_pk_mul_f32 v[196:197], v[200:201], v[196:197]
	s_nop 0
	v_cndmask_b32_e64 v197, v197, -v197, s[4:5]
	v_cndmask_b32_e64 v196, v196, -v196, s[4:5]
	v_pk_fma_f32 v[30:31], v[30:31], v[214:215], v[196:197]
	ds_bpermute_b32 v196, v189, v32
	ds_bpermute_b32 v197, v189, v33
	v_mov_b32_e32 v200, v163
	v_mov_b32_e32 v201, v165
	v_mov_b32_e32 v163, v164
	s_waitcnt lgkmcnt(0)
	v_pk_mul_f32 v[196:197], v[200:201], v[196:197]
	s_nop 0
	v_cndmask_b32_e64 v165, v197, -v197, s[4:5]
	v_cndmask_b32_e64 v164, v196, -v196, s[4:5]
	v_lshl_add_u64 v[196:197], v[186:187], 0, v[192:193]
	v_pk_fma_f32 v[32:33], v[32:33], v[162:163], v[164:165]
	v_add_u32_e32 v238, s100, v196
	ds_read_b128 v[162:165], v238 offset:48
	ds_read_b128 v[214:217], v238 offset:32
	ds_read_b128 v[218:221], v238 offset:16
	ds_read_b128 v[222:225], v238
	ds_bpermute_b32 v200, v189, v22
	ds_bpermute_b32 v201, v189, v23
	s_waitcnt lgkmcnt(0)
	v_mov_b32_e32 v196, v223
	v_mov_b32_e32 v197, v225
	s_waitcnt lgkmcnt(0)
	v_pk_mul_f32 v[196:197], v[196:197], v[200:201]
	v_mov_b32_e32 v223, v224
	v_cndmask_b32_e64 v197, v197, -v197, s[4:5]
	v_cndmask_b32_e64 v196, v196, -v196, s[4:5]
	v_pk_fma_f32 v[22:23], v[22:23], v[222:223], v[196:197]
	ds_bpermute_b32 v196, v189, v24
	ds_bpermute_b32 v197, v189, v25
	v_mov_b32_e32 v200, v219
	v_mov_b32_e32 v201, v221
	v_mov_b32_e32 v219, v220
	s_waitcnt lgkmcnt(0)
	v_pk_mul_f32 v[196:197], v[200:201], v[196:197]
	s_nop 0
	v_cndmask_b32_e64 v197, v197, -v197, s[4:5]
	v_cndmask_b32_e64 v196, v196, -v196, s[4:5]
	v_pk_fma_f32 v[24:25], v[24:25], v[218:219], v[196:197]
	ds_bpermute_b32 v196, v189, v18
	ds_bpermute_b32 v197, v189, v19
	v_mov_b32_e32 v200, v215
	v_mov_b32_e32 v201, v217
	v_mov_b32_e32 v215, v216
	s_waitcnt lgkmcnt(0)
	v_pk_mul_f32 v[196:197], v[200:201], v[196:197]
	s_nop 0
	v_cndmask_b32_e64 v197, v197, -v197, s[4:5]
	v_cndmask_b32_e64 v196, v196, -v196, s[4:5]
	v_pk_fma_f32 v[18:19], v[18:19], v[214:215], v[196:197]
	ds_bpermute_b32 v196, v189, v20
	ds_bpermute_b32 v197, v189, v21
	v_mov_b32_e32 v200, v163
	v_mov_b32_e32 v201, v165
	v_mov_b32_e32 v163, v164
	s_waitcnt lgkmcnt(0)
	v_pk_mul_f32 v[196:197], v[200:201], v[196:197]
	s_nop 0
	v_cndmask_b32_e64 v165, v197, -v197, s[4:5]
	v_cndmask_b32_e64 v164, v196, -v196, s[4:5]
	v_pk_fma_f32 v[20:21], v[20:21], v[162:163], v[164:165]

; template <bool F8OUT = false> __device__ __forceinline__ void head_tile_store(const f32x4 (&acc)[2][2][4][2], bf16_t* obase  , int opitch, const float* gain, float scale, const f32x2e* rope, int row0, int fq) {
;     ...
;             if (rope) {
;                 const int t = row & 8191; const bool second = (fq & 2) != 0;
; #pragma unroll
;                 for (int bj = 0; bj < 2; ++bj) { const int pos = bj ? (t & 63) : (t >> 6); const f32x2e* tb = rope + pos * 16 + 8 * (fq & 1);
; #pragma unroll
;                     for (int n = 0; n < 2; ++n)
; #pragma unroll
;                         for (int e = 0; e < 4; ++e) { const float p = __shfl_xor(x[bj][n][e], 32); const f32x2e cs = tb[4 * n + e]; const float v = x[bj][n][e];
;                             x[bj][n][e] = second ? (p * cs.y + v * cs.x) : (v * cs.x - p * cs.y); } }
;             }
.LBB0_175:
	v_xor_b32_e32 v162, 32, v185
	v_add_u32_e32 v196, 32, v188
	s_and_b64 vcc, exec, s[8:9]
	v_lshlrev_b32_e32 v194, 7, v162
	s_cbranch_vccnz .LBB0_177
	v_and_b32_e32 v163, 64, v212
	v_xor_b32_e32 v162, 32, v212
	v_add_u32_e32 v163, 64, v163
	v_cmp_lt_i32_e32 vcc, v162, v163
	v_mov_b32_e32 v195, v175
	s_nop 0
	v_cndmask_b32_e32 v162, v212, v162, vcc
	v_lshlrev_b32_e32 v185, 2, v162
	v_lshlrev_b32_e32 v162, 1, v196
	v_and_b32_e32 v174, 0x3f80, v162
	v_lshl_add_u64 v[200:201], v[186:187], 0, v[174:175]
	v_add_u32_e32 v238, s100, v200
	ds_read_b128 v[162:165], v238 offset:48
	ds_read_b128 v[214:217], v238 offset:32
	ds_read_b128 v[218:221], v238 offset:16
	ds_read_b128 v[222:225], v238
	ds_bpermute_b32 v226, v185, v26
	ds_bpermute_b32 v227, v185, v27
	s_waitcnt lgkmcnt(0)
	v_mov_b32_e32 v200, v223
	v_mov_b32_e32 v201, v225
	s_waitcnt lgkmcnt(0)
	v_pk_mul_f32 v[200:201], v[200:201], v[226:227]
	v_mov_b32_e32 v223, v224
	v_cndmask_b32_e64 v201, v201, -v201, s[4:5]
	v_cndmask_b32_e64 v200, v200, -v200, s[4:5]
	v_pk_fma_f32 v[26:27], v[26:27], v[222:223], v[200:201]
	ds_bpermute_b32 v200, v185, v28
	ds_bpermute_b32 v201, v185, v29
	v_mov_b32_e32 v222, v219
	v_mov_b32_e32 v223, v221
	v_mov_b32_e32 v219, v220
	ds_bpermute_b32 v226, v185, v22
	s_waitcnt lgkmcnt(1)
	v_pk_mul_f32 v[200:201], v[222:223], v[200:201]
	ds_bpermute_b32 v227, v185, v23
	v_cndmask_b32_e64 v201, v201, -v201, s[4:5]
	v_cndmask_b32_e64 v200, v200, -v200, s[4:5]
	v_pk_fma_f32 v[28:29], v[28:29], v[218:219], v[200:201]
	ds_bpermute_b32 v200, v185, v30
	ds_bpermute_b32 v201, v185, v31
	v_mov_b32_e32 v218, v215
	v_mov_b32_e32 v219, v217
	v_mov_b32_e32 v215, v216
	s_waitcnt lgkmcnt(0)
	v_pk_mul_f32 v[200:201], v[218:219], v[200:201]
	s_nop 0
	v_cndmask_b32_e64 v201, v201, -v201, s[4:5]
	v_cndmask_b32_e64 v200, v200, -v200, s[4:5]
	v_pk_fma_f32 v[30:31], v[30:31], v[214:215], v[200:201]
	ds_bpermute_b32 v200, v185, v32
	ds_bpermute_b32 v201, v185, v33
	v_mov_b32_e32 v214, v163
	v_mov_b32_e32 v215, v165
	v_mov_b32_e32 v163, v164
	s_waitcnt lgkmcnt(0)
	v_pk_mul_f32 v[200:201], v[214:215], v[200:201]
	s_nop 0
	v_cndmask_b32_e64 v165, v201, -v201, s[4:5]
	v_cndmask_b32_e64 v164, v200, -v200, s[4:5]
	v_lshl_add_u64 v[200:201], v[186:187], 0, v[194:195]
	v_pk_fma_f32 v[32:33], v[32:33], v[162:163], v[164:165]
	v_add_u32_e32 v238, s100, v200
	ds_read_b128 v[162:165], v238 offset:48
	ds_read_b128 v[214:217], v238 offset:32
	ds_read_b128 v[218:221], v238 offset:16
	ds_read_b128 v[222:225], v238
	s_waitcnt lgkmcnt(0)
	v_mov_b32_e32 v200, v223
	v_mov_b32_e32 v201, v225
	v_pk_mul_f32 v[200:201], v[200:201], v[226:227]
	v_mov_b32_e32 v223, v224
	v_cndmask_b32_e64 v201, v201, -v201, s[4:5]
	v_cndmask_b32_e64 v200, v200, -v200, s[4:5]
	v_pk_fma_f32 v[22:23], v[22:23], v[222:223], v[200:201]
	ds_bpermute_b32 v200, v185, v24
	ds_bpermute_b32 v201, v185, v25
	v_mov_b32_e32 v222, v219
	v_mov_b32_e32 v223, v221
	v_mov_b32_e32 v219, v220
	s_waitcnt lgkmcnt(0)
	v_pk_mul_f32 v[200:201], v[222:223], v[200:201]
	s_nop 0
	v_cndmask_b32_e64 v201, v201, -v201, s[4:5]
	v_cndmask_b32_e64 v200, v200, -v200, s[4:5]
	v_pk_fma_f32 v[24:25], v[24:25], v[218:219], v[200:201]
	ds_bpermute_b32 v200, v185, v18
	ds_bpermute_b32 v201, v185, v19
	v_mov_b32_e32 v218, v215
	v_mov_b32_e32 v219, v217
	v_mov_b32_e32 v215, v216
	s_waitcnt lgkmcnt(0)
	v_pk_mul_f32 v[200:201], v[218:219], v[200:201]
	s_nop 0
	v_cndmask_b32_e64 v201, v201, -v201, s[4:5]
	v_cndmask_b32_e64 v200, v200, -v200, s[4:5]
	v_pk_fma_f32 v[18:19], v[18:19], v[214:215], v[200:201]
	ds_bpermute_b32 v200, v185, v20
	ds_bpermute_b32 v201, v185, v21
	v_mov_b32_e32 v214, v163
	v_mov_b32_e32 v215, v165
	v_mov_b32_e32 v163, v164
	s_waitcnt lgkmcnt(0)
	v_pk_mul_f32 v[200:201], v[214:215], v[200:201]
	s_nop 0
	v_cndmask_b32_e64 v165, v201, -v201, s[4:5]
	v_cndmask_b32_e64 v164, v200, -v200, s[4:5]
	v_pk_fma_f32 v[20:21], v[20:21], v[162:163], v[164:165]

; template <bool F8OUT = false> __device__ __forceinline__ void head_tile_store(const f32x4 (&acc)[2][2][4][2], bf16_t* obase  , int opitch, const float* gain, float scale, const f32x2e* rope, int row0, int fq) {
;     ...
;             if (rope) {
;                 const int t = row & 8191; const bool second = (fq & 2) != 0;
; #pragma unroll
;                 for (int bj = 0; bj < 2; ++bj) { const int pos = bj ? (t & 63) : (t >> 6); const f32x2e* tb = rope + pos * 16 + 8 * (fq & 1);
; #pragma unroll
;                     for (int n = 0; n < 2; ++n)
; #pragma unroll
;                         for (int e = 0; e < 4; ++e) { const float p = __shfl_xor(x[bj][n][e], 32); const f32x2e cs = tb[4 * n + e]; const float v = x[bj][n][e];
;                             x[bj][n][e] = second ? (p * cs.y + v * cs.x) : (v * cs.x - p * cs.y); } }
;             }
.LBB0_179:
	v_add_u32_e32 v200, 48, v188
	v_and_b32_e32 v162, 63, v200
	s_and_b64 vcc, exec, s[8:9]
	v_lshlrev_b32_e32 v196, 7, v162
	s_cbranch_vccnz .LBB0_181
	v_and_b32_e32 v163, 64, v212
	v_xor_b32_e32 v162, 32, v212
	v_add_u32_e32 v163, 64, v163
	v_cmp_lt_i32_e32 vcc, v162, v163
	v_mov_b32_e32 v197, v175
	s_nop 0
	v_cndmask_b32_e32 v162, v212, v162, vcc
	v_lshlrev_b32_e32 v185, 2, v162
	v_lshlrev_b32_e32 v162, 1, v200
	v_and_b32_e32 v174, 0x3f80, v162
	v_lshl_add_u64 v[222:223], v[186:187], 0, v[174:175]
	v_add_u32_e32 v238, s100, v222
	ds_read_b128 v[162:165], v238 offset:48
	ds_read_b128 v[214:217], v238 offset:32
	ds_read_b128 v[218:221], v238 offset:16
	ds_read_b128 v[222:225], v238
	ds_bpermute_b32 v226, v185, v26
	ds_bpermute_b32 v227, v185, v27
	s_waitcnt lgkmcnt(0)
	v_mov_b32_e32 v228, v223
	v_mov_b32_e32 v229, v225
	s_waitcnt lgkmcnt(0)
	v_pk_mul_f32 v[226:227], v[228:229], v[226:227]
	v_mov_b32_e32 v223, v224
	v_cndmask_b32_e64 v225, v227, -v227, s[4:5]
	v_cndmask_b32_e64 v224, v226, -v226, s[4:5]
	v_pk_fma_f32 v[26:27], v[26:27], v[222:223], v[224:225]
	ds_bpermute_b32 v222, v185, v28
	ds_bpermute_b32 v223, v185, v29
	v_mov_b32_e32 v224, v219
	v_mov_b32_e32 v225, v221
	v_mov_b32_e32 v219, v220
	ds_bpermute_b32 v226, v185, v22
	s_waitcnt lgkmcnt(1)
	v_pk_mul_f32 v[222:223], v[224:225], v[222:223]
	ds_bpermute_b32 v227, v185, v23
	v_cndmask_b32_e64 v221, v223, -v223, s[4:5]
	v_cndmask_b32_e64 v220, v222, -v222, s[4:5]
	v_pk_fma_f32 v[28:29], v[28:29], v[218:219], v[220:221]
	ds_bpermute_b32 v218, v185, v30
	ds_bpermute_b32 v219, v185, v31
	v_mov_b32_e32 v220, v215
	v_mov_b32_e32 v221, v217
	v_mov_b32_e32 v215, v216
	v_lshl_add_u64 v[222:223], v[186:187], 0, v[196:197]
	s_waitcnt lgkmcnt(0)
	v_pk_mul_f32 v[218:219], v[220:221], v[218:219]
	s_nop 0
	v_cndmask_b32_e64 v217, v219, -v219, s[4:5]
	v_cndmask_b32_e64 v216, v218, -v218, s[4:5]
	v_pk_fma_f32 v[30:31], v[30:31], v[214:215], v[216:217]
	ds_bpermute_b32 v214, v185, v32
	ds_bpermute_b32 v215, v185, v33
	v_mov_b32_e32 v216, v163
	v_mov_b32_e32 v217, v165
	v_mov_b32_e32 v163, v164
	s_waitcnt lgkmcnt(0)
	v_pk_mul_f32 v[214:215], v[216:217], v[214:215]
	s_nop 0
	v_cndmask_b32_e64 v165, v215, -v215, s[4:5]
	v_cndmask_b32_e64 v164, v214, -v214, s[4:5]
	v_pk_fma_f32 v[32:33], v[32:33], v[162:163], v[164:165]
	v_add_u32_e32 v238, s100, v222
	ds_read_b128 v[162:165], v238 offset:48
	ds_read_b128 v[214:217], v238 offset:32
	ds_read_b128 v[218:221], v238 offset:16
	ds_read_b128 v[222:225], v238
	s_waitcnt lgkmcnt(0)
	v_mov_b32_e32 v228, v223
	v_mov_b32_e32 v229, v225
	v_pk_mul_f32 v[226:227], v[228:229], v[226:227]
	v_mov_b32_e32 v223, v224
	v_cndmask_b32_e64 v225, v227, -v227, s[4:5]
	v_cndmask_b32_e64 v224, v226, -v226, s[4:5]
	v_pk_fma_f32 v[22:23], v[22:23], v[222:223], v[224:225]
	ds_bpermute_b32 v222, v185, v24
	ds_bpermute_b32 v223, v185, v25
	v_mov_b32_e32 v224, v219
	v_mov_b32_e32 v225, v221
	v_mov_b32_e32 v219, v220
	s_waitcnt lgkmcnt(0)
	v_pk_mul_f32 v[222:223], v[224:225], v[222:223]
	s_nop 0
	v_cndmask_b32_e64 v221, v223, -v223, s[4:5]
	v_cndmask_b32_e64 v220, v222, -v222, s[4:5]
	v_pk_fma_f32 v[24:25], v[24:25], v[218:219], v[220:221]
	ds_bpermute_b32 v218, v185, v18
	ds_bpermute_b32 v219, v185, v19
	v_mov_b32_e32 v220, v215
	v_mov_b32_e32 v221, v217
	v_mov_b32_e32 v215, v216
	s_waitcnt lgkmcnt(0)
	v_pk_mul_f32 v[218:219], v[220:221], v[218:219]
	s_nop 0
	v_cndmask_b32_e64 v217, v219, -v219, s[4:5]
	v_cndmask_b32_e64 v216, v218, -v218, s[4:5]
	v_pk_fma_f32 v[18:19], v[18:19], v[214:215], v[216:217]
	ds_bpermute_b32 v214, v185, v20
	ds_bpermute_b32 v215, v185, v21
	v_mov_b32_e32 v216, v163
	v_mov_b32_e32 v217, v165
	v_mov_b32_e32 v163, v164
	s_waitcnt lgkmcnt(0)
	v_pk_mul_f32 v[214:215], v[216:217], v[214:215]
	s_nop 0
	v_cndmask_b32_e64 v165, v215, -v215, s[4:5]
	v_cndmask_b32_e64 v164, v214, -v214, s[4:5]
	v_pk_fma_f32 v[20:21], v[20:21], v[162:163], v[164:165]

; template <bool F8OUT = false> __device__ __forceinline__ void head_tile_store(const f32x4 (&acc)[2][2][4][2], bf16_t* obase  , int opitch, const float* gain, float scale, const f32x2e* rope, int row0, int fq) {
;     ...
;             if (rope) {
;                 const int t = row & 8191; const bool second = (fq & 2) != 0;
; #pragma unroll
;                 for (int bj = 0; bj < 2; ++bj) { const int pos = bj ? (t & 63) : (t >> 6); const f32x2e* tb = rope + pos * 16 + 8 * (fq & 1);
; #pragma unroll
;                     for (int n = 0; n < 2; ++n)
; #pragma unroll
;                         for (int e = 0; e < 4; ++e) { const float p = __shfl_xor(x[bj][n][e], 32); const f32x2e cs = tb[4 * n + e]; const float v = x[bj][n][e];
;                             x[bj][n][e] = second ? (p * cs.y + v * cs.x) : (v * cs.x - p * cs.y); } }
;             }
.LBB0_183:
	s_and_b64 vcc, exec, s[8:9]
	v_add_u32_e32 v200, 0x80, v188
	s_cbranch_vccnz .LBB0_185
	v_and_b32_e32 v163, 64, v212
	v_xor_b32_e32 v162, 32, v212
	v_add_u32_e32 v163, 64, v163
	v_cmp_lt_i32_e32 vcc, v162, v163
	v_mov_b32_e32 v199, v175
	v_lshl_add_u64 v[198:199], v[186:187], 0, v[198:199]
	v_cndmask_b32_e32 v162, v212, v162, vcc
	v_lshlrev_b32_e32 v185, 2, v162
	v_lshlrev_b32_e32 v162, 1, v200
	v_and_b32_e32 v174, 0x3f80, v162
	v_lshl_add_u64 v[222:223], v[186:187], 0, v[174:175]
	v_add_u32_e32 v238, s100, v222
	ds_read_b128 v[162:165], v238 offset:48
	ds_read_b128 v[214:217], v238 offset:32
	ds_read_b128 v[218:221], v238 offset:16
	ds_read_b128 v[222:225], v238
	ds_bpermute_b32 v226, v185, v26
	ds_bpermute_b32 v227, v185, v27
	s_waitcnt lgkmcnt(0)
	v_mov_b32_e32 v228, v223
	v_mov_b32_e32 v229, v225
	s_waitcnt lgkmcnt(0)
	v_pk_mul_f32 v[226:227], v[228:229], v[226:227]
	v_mov_b32_e32 v223, v224
	v_cndmask_b32_e64 v225, v227, -v227, s[4:5]
	v_cndmask_b32_e64 v224, v226, -v226, s[4:5]
	v_pk_fma_f32 v[26:27], v[26:27], v[222:223], v[224:225]
	ds_bpermute_b32 v222, v185, v28
	ds_bpermute_b32 v223, v185, v29
	v_mov_b32_e32 v224, v219
	v_mov_b32_e32 v225, v221
	v_mov_b32_e32 v219, v220
	ds_bpermute_b32 v226, v185, v22
	s_waitcnt lgkmcnt(1)
	v_pk_mul_f32 v[222:223], v[224:225], v[222:223]
	ds_bpermute_b32 v227, v185, v23
	v_cndmask_b32_e64 v221, v223, -v223, s[4:5]
	v_cndmask_b32_e64 v220, v222, -v222, s[4:5]
	v_pk_fma_f32 v[28:29], v[28:29], v[218:219], v[220:221]
	ds_bpermute_b32 v218, v185, v30
	ds_bpermute_b32 v219, v185, v31
	v_mov_b32_e32 v220, v215
	v_mov_b32_e32 v221, v217
	v_mov_b32_e32 v215, v216
	s_waitcnt lgkmcnt(0)
	v_pk_mul_f32 v[218:219], v[220:221], v[218:219]
	s_nop 0
	v_cndmask_b32_e64 v217, v219, -v219, s[4:5]
	v_cndmask_b32_e64 v216, v218, -v218, s[4:5]
	v_pk_fma_f32 v[30:31], v[30:31], v[214:215], v[216:217]
	ds_bpermute_b32 v214, v185, v32
	ds_bpermute_b32 v215, v185, v33
	v_mov_b32_e32 v216, v163
	v_mov_b32_e32 v217, v165
	v_mov_b32_e32 v163, v164
	s_waitcnt lgkmcnt(0)
	v_pk_mul_f32 v[214:215], v[216:217], v[214:215]
	s_nop 0
	v_cndmask_b32_e64 v165, v215, -v215, s[4:5]
	v_cndmask_b32_e64 v164, v214, -v214, s[4:5]
	v_pk_fma_f32 v[32:33], v[32:33], v[162:163], v[164:165]
	v_add_u32_e32 v238, s100, v198
	ds_read_b128 v[162:165], v238 offset:48
	ds_read_b128 v[214:217], v238 offset:32
	ds_read_b128 v[218:221], v238 offset:16
	ds_read_b128 v[222:225], v238
	s_waitcnt lgkmcnt(0)
	v_mov_b32_e32 v198, v223
	v_mov_b32_e32 v199, v225
	v_pk_mul_f32 v[198:199], v[198:199], v[226:227]
	v_mov_b32_e32 v223, v224
	v_cndmask_b32_e64 v199, v199, -v199, s[4:5]
	v_cndmask_b32_e64 v198, v198, -v198, s[4:5]
	v_pk_fma_f32 v[22:23], v[22:23], v[222:223], v[198:199]
	ds_bpermute_b32 v198, v185, v24
	ds_bpermute_b32 v199, v185, v25
	v_mov_b32_e32 v222, v219
	v_mov_b32_e32 v223, v221
	v_mov_b32_e32 v219, v220
	s_waitcnt lgkmcnt(0)
	v_pk_mul_f32 v[198:199], v[222:223], v[198:199]
	s_nop 0
	v_cndmask_b32_e64 v199, v199, -v199, s[4:5]
	v_cndmask_b32_e64 v198, v198, -v198, s[4:5]
	v_pk_fma_f32 v[24:25], v[24:25], v[218:219], v[198:199]
	ds_bpermute_b32 v198, v185, v18
	ds_bpermute_b32 v199, v185, v19
	v_mov_b32_e32 v218, v215
	v_mov_b32_e32 v219, v217
	v_mov_b32_e32 v215, v216
	s_waitcnt lgkmcnt(0)
	v_pk_mul_f32 v[198:199], v[218:219], v[198:199]
	s_nop 0
	v_cndmask_b32_e64 v199, v199, -v199, s[4:5]
	v_cndmask_b32_e64 v198, v198, -v198, s[4:5]
	v_pk_fma_f32 v[18:19], v[18:19], v[214:215], v[198:199]
	ds_bpermute_b32 v198, v185, v20
	ds_bpermute_b32 v199, v185, v21
	v_mov_b32_e32 v214, v163
	v_mov_b32_e32 v215, v165
	v_mov_b32_e32 v163, v164
	s_waitcnt lgkmcnt(0)
	v_pk_mul_f32 v[198:199], v[214:215], v[198:199]
	s_nop 0
	v_cndmask_b32_e64 v165, v199, -v199, s[4:5]
	v_cndmask_b32_e64 v164, v198, -v198, s[4:5]
	v_pk_fma_f32 v[20:21], v[20:21], v[162:163], v[164:165]

; template <bool F8OUT = false> __device__ __forceinline__ void head_tile_store(const f32x4 (&acc)[2][2][4][2], bf16_t* obase  , int opitch, const float* gain, float scale, const f32x2e* rope, int row0, int fq) {
;     ...
;             if (rope) {
;                 const int t = row & 8191; const bool second = (fq & 2) != 0;
; #pragma unroll
;                 for (int bj = 0; bj < 2; ++bj) { const int pos = bj ? (t & 63) : (t >> 6); const f32x2e* tb = rope + pos * 16 + 8 * (fq & 1);
; #pragma unroll
;                     for (int n = 0; n < 2; ++n)
; #pragma unroll
;                         for (int e = 0; e < 4; ++e) { const float p = __shfl_xor(x[bj][n][e], 32); const f32x2e cs = tb[4 * n + e]; const float v = x[bj][n][e];
;                             x[bj][n][e] = second ? (p * cs.y + v * cs.x) : (v * cs.x - p * cs.y); } }
;             }
.LBB0_187:
	s_and_b64 vcc, exec, s[8:9]
	v_add_u32_e32 v198, 0x90, v188
	s_cbranch_vccnz .LBB0_189
	v_and_b32_e32 v163, 64, v212
	v_xor_b32_e32 v162, 32, v212
	v_add_u32_e32 v163, 64, v163
	v_cmp_lt_i32_e32 vcc, v162, v163
	v_mov_b32_e32 v193, v175
	v_lshl_add_u64 v[192:193], v[186:187], 0, v[192:193]
	v_cndmask_b32_e32 v162, v212, v162, vcc
	v_lshlrev_b32_e32 v185, 2, v162
	v_lshlrev_b32_e32 v162, 1, v198
	v_and_b32_e32 v174, 0x3f80, v162
	v_lshl_add_u64 v[200:201], v[186:187], 0, v[174:175]
	v_add_u32_e32 v238, s100, v200
	ds_read_b128 v[162:165], v238 offset:48
	ds_read_b128 v[214:217], v238 offset:32
	ds_read_b128 v[218:221], v238 offset:16
	ds_read_b128 v[222:225], v238
	ds_bpermute_b32 v226, v185, v26
	ds_bpermute_b32 v227, v185, v27
	s_waitcnt lgkmcnt(0)
	v_mov_b32_e32 v200, v223
	v_mov_b32_e32 v201, v225
	s_waitcnt lgkmcnt(0)
	v_pk_mul_f32 v[200:201], v[200:201], v[226:227]
	v_mov_b32_e32 v223, v224
	v_cndmask_b32_e64 v201, v201, -v201, s[4:5]
	v_cndmask_b32_e64 v200, v200, -v200, s[4:5]
	v_pk_fma_f32 v[26:27], v[26:27], v[222:223], v[200:201]
	ds_bpermute_b32 v200, v185, v28
	ds_bpermute_b32 v201, v185, v29
	v_mov_b32_e32 v222, v219
	v_mov_b32_e32 v223, v221
	v_mov_b32_e32 v219, v220
	s_waitcnt lgkmcnt(0)
	v_pk_mul_f32 v[200:201], v[222:223], v[200:201]
	s_nop 0
	v_cndmask_b32_e64 v201, v201, -v201, s[4:5]
	v_cndmask_b32_e64 v200, v200, -v200, s[4:5]
	v_pk_fma_f32 v[28:29], v[28:29], v[218:219], v[200:201]
	ds_bpermute_b32 v200, v185, v30
	ds_bpermute_b32 v201, v185, v31
	v_mov_b32_e32 v218, v215
	v_mov_b32_e32 v219, v217
	v_mov_b32_e32 v215, v216
	s_waitcnt lgkmcnt(0)
	v_pk_mul_f32 v[200:201], v[218:219], v[200:201]
	s_nop 0
	v_cndmask_b32_e64 v201, v201, -v201, s[4:5]
	v_cndmask_b32_e64 v200, v200, -v200, s[4:5]
	v_pk_fma_f32 v[30:31], v[30:31], v[214:215], v[200:201]
	ds_bpermute_b32 v200, v185, v32
	ds_bpermute_b32 v201, v185, v33
	v_mov_b32_e32 v214, v163
	v_mov_b32_e32 v215, v165
	v_mov_b32_e32 v163, v164
	s_waitcnt lgkmcnt(0)
	v_pk_mul_f32 v[200:201], v[214:215], v[200:201]
	s_nop 0
	v_cndmask_b32_e64 v165, v201, -v201, s[4:5]
	v_cndmask_b32_e64 v164, v200, -v200, s[4:5]
	v_pk_fma_f32 v[32:33], v[32:33], v[162:163], v[164:165]
	v_add_u32_e32 v238, s100, v192
	ds_read_b128 v[162:165], v238 offset:48
	ds_read_b128 v[214:217], v238 offset:32
	ds_read_b128 v[218:221], v238 offset:16
	ds_read_b128 v[222:225], v238
	ds_bpermute_b32 v200, v185, v22
	ds_bpermute_b32 v201, v185, v23
	s_waitcnt lgkmcnt(0)
	v_mov_b32_e32 v192, v223
	v_mov_b32_e32 v193, v225
	s_waitcnt lgkmcnt(0)
	v_pk_mul_f32 v[192:193], v[192:193], v[200:201]
	v_mov_b32_e32 v223, v224
	v_cndmask_b32_e64 v193, v193, -v193, s[4:5]
	v_cndmask_b32_e64 v192, v192, -v192, s[4:5]
	v_pk_fma_f32 v[22:23], v[22:23], v[222:223], v[192:193]
	ds_bpermute_b32 v192, v185, v24
	ds_bpermute_b32 v193, v185, v25
	v_mov_b32_e32 v200, v219
	v_mov_b32_e32 v201, v221
	v_mov_b32_e32 v219, v220
	s_waitcnt lgkmcnt(0)
	v_pk_mul_f32 v[192:193], v[200:201], v[192:193]
	s_nop 0
	v_cndmask_b32_e64 v193, v193, -v193, s[4:5]
	v_cndmask_b32_e64 v192, v192, -v192, s[4:5]
	v_pk_fma_f32 v[24:25], v[24:25], v[218:219], v[192:193]
	ds_bpermute_b32 v192, v185, v18
	ds_bpermute_b32 v193, v185, v19
	v_mov_b32_e32 v200, v215
	v_mov_b32_e32 v201, v217
	v_mov_b32_e32 v215, v216
	s_waitcnt lgkmcnt(0)
	v_pk_mul_f32 v[192:193], v[200:201], v[192:193]
	s_nop 0
	v_cndmask_b32_e64 v193, v193, -v193, s[4:5]
	v_cndmask_b32_e64 v192, v192, -v192, s[4:5]
	v_pk_fma_f32 v[18:19], v[18:19], v[214:215], v[192:193]
	ds_bpermute_b32 v192, v185, v20
	ds_bpermute_b32 v193, v185, v21
	v_mov_b32_e32 v200, v163
	v_mov_b32_e32 v201, v165
	v_mov_b32_e32 v163, v164
	s_waitcnt lgkmcnt(0)
	v_pk_mul_f32 v[192:193], v[200:201], v[192:193]
	s_nop 0
	v_cndmask_b32_e64 v165, v193, -v193, s[4:5]
	v_cndmask_b32_e64 v164, v192, -v192, s[4:5]
	v_pk_fma_f32 v[20:21], v[20:21], v[162:163], v[164:165]

; template <bool F8OUT = false> __device__ __forceinline__ void head_tile_store(const f32x4 (&acc)[2][2][4][2], bf16_t* obase  , int opitch, const float* gain, float scale, const f32x2e* rope, int row0, int fq) {
;     ...
;             if (rope) {
;                 const int t = row & 8191; const bool second = (fq & 2) != 0;
; #pragma unroll
;                 for (int bj = 0; bj < 2; ++bj) { const int pos = bj ? (t & 63) : (t >> 6); const f32x2e* tb = rope + pos * 16 + 8 * (fq & 1);
; #pragma unroll
;                     for (int n = 0; n < 2; ++n)
; #pragma unroll
;                         for (int e = 0; e < 4; ++e) { const float p = __shfl_xor(x[bj][n][e], 32); const f32x2e cs = tb[4 * n + e]; const float v = x[bj][n][e];
;                             x[bj][n][e] = second ? (p * cs.y + v * cs.x) : (v * cs.x - p * cs.y); } }
;             }
.LBB0_191:
	s_and_b64 vcc, exec, s[8:9]
	v_add_u32_e32 v192, 0xa0, v188
	s_cbranch_vccnz .LBB0_193
	v_and_b32_e32 v163, 64, v212
	v_xor_b32_e32 v162, 32, v212
	v_add_u32_e32 v163, 64, v163
	v_cmp_lt_i32_e32 vcc, v162, v163
	v_mov_b32_e32 v195, v175
	v_lshl_add_u64 v[194:195], v[186:187], 0, v[194:195]
	v_cndmask_b32_e32 v162, v212, v162, vcc
	v_lshlrev_b32_e32 v185, 2, v162
	v_lshlrev_b32_e32 v162, 1, v192
	v_and_b32_e32 v174, 0x3f80, v162
	v_lshl_add_u64 v[218:219], v[186:187], 0, v[174:175]
	v_add_u32_e32 v238, s100, v218
	ds_read_b128 v[162:165], v238 offset:48
	ds_read_b128 v[198:201], v238 offset:32
	ds_read_b128 v[214:217], v238 offset:16
	ds_read_b128 v[218:221], v238
	ds_bpermute_b32 v222, v185, v26
	ds_bpermute_b32 v223, v185, v27
	s_waitcnt lgkmcnt(0)
	v_mov_b32_e32 v224, v219
	v_mov_b32_e32 v225, v221
	s_waitcnt lgkmcnt(0)
	v_pk_mul_f32 v[222:223], v[224:225], v[222:223]
	v_mov_b32_e32 v219, v220
	v_cndmask_b32_e64 v221, v223, -v223, s[4:5]
	v_cndmask_b32_e64 v220, v222, -v222, s[4:5]
	v_pk_fma_f32 v[26:27], v[26:27], v[218:219], v[220:221]
	ds_bpermute_b32 v218, v185, v28
	ds_bpermute_b32 v219, v185, v29
	v_mov_b32_e32 v220, v215
	v_mov_b32_e32 v221, v217
	v_mov_b32_e32 v215, v216
	ds_bpermute_b32 v222, v185, v22
	s_waitcnt lgkmcnt(1)
	v_pk_mul_f32 v[218:219], v[220:221], v[218:219]
	ds_bpermute_b32 v223, v185, v23
	v_cndmask_b32_e64 v217, v219, -v219, s[4:5]
	v_cndmask_b32_e64 v216, v218, -v218, s[4:5]
	v_pk_fma_f32 v[28:29], v[28:29], v[214:215], v[216:217]
	ds_bpermute_b32 v214, v185, v30
	ds_bpermute_b32 v215, v185, v31
	v_mov_b32_e32 v216, v199
	v_mov_b32_e32 v217, v201
	v_mov_b32_e32 v199, v200
	s_waitcnt lgkmcnt(0)
	v_pk_mul_f32 v[214:215], v[216:217], v[214:215]
	s_nop 0
	v_cndmask_b32_e64 v201, v215, -v215, s[4:5]
	v_cndmask_b32_e64 v200, v214, -v214, s[4:5]
	v_pk_fma_f32 v[30:31], v[30:31], v[198:199], v[200:201]
	ds_bpermute_b32 v198, v185, v32
	ds_bpermute_b32 v199, v185, v33
	v_mov_b32_e32 v200, v163
	v_mov_b32_e32 v201, v165
	v_mov_b32_e32 v163, v164
	s_waitcnt lgkmcnt(0)
	v_pk_mul_f32 v[198:199], v[200:201], v[198:199]
	s_nop 0
	v_cndmask_b32_e64 v165, v199, -v199, s[4:5]
	v_cndmask_b32_e64 v164, v198, -v198, s[4:5]
	v_pk_fma_f32 v[32:33], v[32:33], v[162:163], v[164:165]
	v_add_u32_e32 v238, s100, v194
	ds_read_b128 v[162:165], v238 offset:48
	ds_read_b128 v[198:201], v238 offset:32
	ds_read_b128 v[214:217], v238 offset:16
	ds_read_b128 v[218:221], v238
	s_waitcnt lgkmcnt(0)
	v_mov_b32_e32 v194, v219
	v_mov_b32_e32 v195, v221
	v_pk_mul_f32 v[194:195], v[194:195], v[222:223]
	v_mov_b32_e32 v219, v220
	v_cndmask_b32_e64 v195, v195, -v195, s[4:5]
	v_cndmask_b32_e64 v194, v194, -v194, s[4:5]
	v_pk_fma_f32 v[22:23], v[22:23], v[218:219], v[194:195]
	ds_bpermute_b32 v194, v185, v24
	ds_bpermute_b32 v195, v185, v25
	v_mov_b32_e32 v218, v215
	v_mov_b32_e32 v219, v217
	v_mov_b32_e32 v215, v216
	s_waitcnt lgkmcnt(0)
	v_pk_mul_f32 v[194:195], v[218:219], v[194:195]
	s_nop 0
	v_cndmask_b32_e64 v195, v195, -v195, s[4:5]
	v_cndmask_b32_e64 v194, v194, -v194, s[4:5]
	v_pk_fma_f32 v[24:25], v[24:25], v[214:215], v[194:195]
	ds_bpermute_b32 v194, v185, v18
	ds_bpermute_b32 v195, v185, v19
	v_mov_b32_e32 v214, v199
	v_mov_b32_e32 v215, v201
	v_mov_b32_e32 v199, v200
	s_waitcnt lgkmcnt(0)
	v_pk_mul_f32 v[194:195], v[214:215], v[194:195]
	s_nop 0
	v_cndmask_b32_e64 v195, v195, -v195, s[4:5]
	v_cndmask_b32_e64 v194, v194, -v194, s[4:5]
	v_pk_fma_f32 v[18:19], v[18:19], v[198:199], v[194:195]
	ds_bpermute_b32 v194, v185, v20
	ds_bpermute_b32 v195, v185, v21
	v_mov_b32_e32 v198, v163
	v_mov_b32_e32 v199, v165
	v_mov_b32_e32 v163, v164
	s_waitcnt lgkmcnt(0)
	v_pk_mul_f32 v[194:195], v[198:199], v[194:195]
	s_nop 0
	v_cndmask_b32_e64 v165, v195, -v195, s[4:5]
	v_cndmask_b32_e64 v164, v194, -v194, s[4:5]
	v_pk_fma_f32 v[20:21], v[20:21], v[162:163], v[164:165]

; template <bool F8OUT = false> __device__ __forceinline__ void head_tile_store(const f32x4 (&acc)[2][2][4][2], bf16_t* obase  , int opitch, const float* gain, float scale, const f32x2e* rope, int row0, int fq) {
;     ...
;             if (rope) {
;                 const int t = row & 8191; const bool second = (fq & 2) != 0;
; #pragma unroll
;                 for (int bj = 0; bj < 2; ++bj) { const int pos = bj ? (t & 63) : (t >> 6); const f32x2e* tb = rope + pos * 16 + 8 * (fq & 1);
; #pragma unroll
;                     for (int n = 0; n < 2; ++n)
; #pragma unroll
;                         for (int e = 0; e < 4; ++e) { const float p = __shfl_xor(x[bj][n][e], 32); const f32x2e cs = tb[4 * n + e]; const float v = x[bj][n][e];
;                             x[bj][n][e] = second ? (p * cs.y + v * cs.x) : (v * cs.x - p * cs.y); } }
;             }
.LBB0_195:
	s_and_b64 vcc, exec, s[8:9]
	s_waitcnt vmcnt(0)
	v_add_u32_e32 v6, 0xb0, v188
	s_cbranch_vccnz .LBB0_197
	v_and_b32_e32 v3, 64, v212
	v_xor_b32_e32 v2, 32, v212
	v_add_u32_e32 v3, 64, v3
	v_cmp_lt_i32_e32 vcc, v2, v3
	v_mov_b32_e32 v197, v175
	s_nop 0
	v_cndmask_b32_e32 v2, v212, v2, vcc
	v_lshlrev_b32_e32 v7, 2, v2
	v_lshlrev_b32_e32 v2, 1, v6
	v_and_b32_e32 v174, 0x3f80, v2
	v_lshl_add_u64 v[16:17], v[186:187], 0, v[174:175]
	v_add_u32_e32 v238, s100, v16
	ds_read_b128 v[2:5], v238 offset:48
	ds_read_b128 v[8:11], v238 offset:32
	ds_read_b128 v[12:15], v238 offset:16
	ds_read_b128 v[162:165], v238
	ds_bpermute_b32 v188, v7, v26
	ds_bpermute_b32 v189, v7, v27
	s_waitcnt lgkmcnt(0)
	v_mov_b32_e32 v16, v163
	v_mov_b32_e32 v17, v165
	s_waitcnt lgkmcnt(0)
	v_pk_mul_f32 v[16:17], v[16:17], v[188:189]
	v_mov_b32_e32 v163, v164
	v_cndmask_b32_e64 v17, v17, -v17, s[4:5]
	v_cndmask_b32_e64 v16, v16, -v16, s[4:5]
	v_pk_fma_f32 v[26:27], v[26:27], v[162:163], v[16:17]
	ds_bpermute_b32 v16, v7, v28
	ds_bpermute_b32 v17, v7, v29
	v_mov_b32_e32 v162, v13
	v_mov_b32_e32 v163, v15
	v_mov_b32_e32 v13, v14
	s_waitcnt lgkmcnt(0)
	v_pk_mul_f32 v[16:17], v[162:163], v[16:17]
	s_nop 0
	v_cndmask_b32_e64 v15, v17, -v17, s[4:5]
	v_cndmask_b32_e64 v14, v16, -v16, s[4:5]
	v_pk_fma_f32 v[28:29], v[28:29], v[12:13], v[14:15]
	ds_bpermute_b32 v12, v7, v30
	ds_bpermute_b32 v13, v7, v31
	v_mov_b32_e32 v14, v9
	v_mov_b32_e32 v15, v11
	v_mov_b32_e32 v9, v10
	v_lshl_add_u64 v[16:17], v[186:187], 0, v[196:197]
	s_waitcnt lgkmcnt(0)
	v_pk_mul_f32 v[12:13], v[14:15], v[12:13]
	ds_bpermute_b32 v186, v7, v22
	v_cndmask_b32_e64 v11, v13, -v13, s[4:5]
	v_cndmask_b32_e64 v10, v12, -v12, s[4:5]
	v_pk_fma_f32 v[30:31], v[30:31], v[8:9], v[10:11]
	ds_bpermute_b32 v8, v7, v32
	ds_bpermute_b32 v9, v7, v33
	v_mov_b32_e32 v10, v3
	v_mov_b32_e32 v11, v5
	v_mov_b32_e32 v3, v4
	ds_bpermute_b32 v187, v7, v23
	s_waitcnt lgkmcnt(1)
	v_pk_mul_f32 v[8:9], v[10:11], v[8:9]
	s_nop 0
	v_cndmask_b32_e64 v5, v9, -v9, s[4:5]
	v_cndmask_b32_e64 v4, v8, -v8, s[4:5]
	v_pk_fma_f32 v[32:33], v[32:33], v[2:3], v[4:5]
	v_add_u32_e32 v238, s100, v16
	ds_read_b128 v[2:5], v238 offset:48
	ds_read_b128 v[8:11], v238 offset:32
	ds_read_b128 v[12:15], v238 offset:16
	ds_read_b128 v[162:165], v238
	s_waitcnt lgkmcnt(0)
	v_mov_b32_e32 v16, v163
	v_mov_b32_e32 v17, v165
	s_waitcnt lgkmcnt(0)
	v_pk_mul_f32 v[16:17], v[16:17], v[186:187]
	v_mov_b32_e32 v163, v164
	v_cndmask_b32_e64 v17, v17, -v17, s[4:5]
	v_cndmask_b32_e64 v16, v16, -v16, s[4:5]
	v_pk_fma_f32 v[22:23], v[22:23], v[162:163], v[16:17]
	ds_bpermute_b32 v16, v7, v24
	ds_bpermute_b32 v17, v7, v25
	v_mov_b32_e32 v162, v13
	v_mov_b32_e32 v163, v15
	v_mov_b32_e32 v13, v14
	s_waitcnt lgkmcnt(0)
	v_pk_mul_f32 v[16:17], v[162:163], v[16:17]
	s_nop 0
	v_cndmask_b32_e64 v15, v17, -v17, s[4:5]
	v_cndmask_b32_e64 v14, v16, -v16, s[4:5]
	v_pk_fma_f32 v[24:25], v[24:25], v[12:13], v[14:15]
	ds_bpermute_b32 v12, v7, v18
	ds_bpermute_b32 v13, v7, v19
	v_mov_b32_e32 v14, v9
	v_mov_b32_e32 v15, v11
	v_mov_b32_e32 v9, v10
	s_waitcnt lgkmcnt(0)
	v_pk_mul_f32 v[12:13], v[14:15], v[12:13]
	s_nop 0
	v_cndmask_b32_e64 v11, v13, -v13, s[4:5]
	v_cndmask_b32_e64 v10, v12, -v12, s[4:5]
	v_pk_fma_f32 v[18:19], v[18:19], v[8:9], v[10:11]
	ds_bpermute_b32 v8, v7, v20
	ds_bpermute_b32 v9, v7, v21
	v_mov_b32_e32 v10, v3
	v_mov_b32_e32 v11, v5
	v_mov_b32_e32 v3, v4
	s_waitcnt lgkmcnt(0)
	v_pk_mul_f32 v[8:9], v[10:11], v[8:9]
	s_nop 0
	v_cndmask_b32_e64 v5, v9, -v9, s[4:5]
	v_cndmask_b32_e64 v4, v8, -v8, s[4:5]
	v_pk_fma_f32 v[20:21], v[20:21], v[2:3], v[4:5]

; __global__ void __launch_bounds__(NWAVES * 64, 2) enc_fwd(Args args) {
	.amdhsa_kernel _Z7enc_fwd4Args
		.amdhsa_group_segment_fixed_size 0
		.amdhsa_private_segment_fixed_size 0
		.amdhsa_kernarg_size 480
		.amdhsa_user_sgpr_count 2
		.amdhsa_user_sgpr_dispatch_ptr 0
		.amdhsa_user_sgpr_queue_ptr 0
		.amdhsa_user_sgpr_kernarg_segment_ptr 1
		.amdhsa_user_sgpr_dispatch_id 0
		.amdhsa_user_sgpr_kernarg_preload_length 0
		.amdhsa_user_sgpr_kernarg_preload_offset 0
		.amdhsa_user_sgpr_private_segment_size 0
		.amdhsa_uses_dynamic_stack 0
		.amdhsa_enable_private_segment 0
		.amdhsa_system_sgpr_workgroup_id_x 1
		.amdhsa_system_sgpr_workgroup_id_y 0
		.amdhsa_system_sgpr_workgroup_id_z 0
		.amdhsa_system_sgpr_workgroup_info 0
		.amdhsa_system_vgpr_workitem_id 0
		.amdhsa_next_free_vgpr 256
		.amdhsa_next_free_sgpr 102
		.amdhsa_accum_offset 256
		.amdhsa_reserve_vcc 1
		.amdhsa_float_round_mode_32 0
		.amdhsa_float_round_mode_16_64 0
		.amdhsa_float_denorm_mode_32 3
		.amdhsa_float_denorm_mode_16_64 3
		.amdhsa_dx10_clamp 1
		.amdhsa_ieee_mode 1
		.amdhsa_fp16_overflow 0
		.amdhsa_tg_split 0
		.amdhsa_exception_fp_ieee_invalid_op 0
		.amdhsa_exception_fp_denorm_src 0
		.amdhsa_exception_fp_ieee_div_zero 0
		.amdhsa_exception_fp_ieee_overflow 0
		.amdhsa_exception_fp_ieee_underflow 0
		.amdhsa_exception_fp_ieee_inexact 0
		.amdhsa_exception_int_div_zero 0
	.end_amdhsa_kernel

; __global__ void __launch_bounds__(NWAVES * 64, 2) enc_fwd(Args args) {
amdhsa.kernels:
  - .agpr_count:     0
    .args:
      - .offset:         0
        .size:           224
        .value_kind:     by_value
      - .offset:         224
        .size:           4
        .value_kind:     hidden_block_count_x
      - .offset:         228
        .size:           4
        .value_kind:     hidden_block_count_y
      - .offset:         232
        .size:           4
        .value_kind:     hidden_block_count_z
      - .offset:         236
        .size:           2
        .value_kind:     hidden_group_size_x
      - .offset:         238
        .size:           2
        .value_kind:     hidden_group_size_y
      - .offset:         240
        .size:           2
        .value_kind:     hidden_group_size_z
      - .offset:         242
        .size:           2
        .value_kind:     hidden_remainder_x
      - .offset:         244
        .size:           2
        .value_kind:     hidden_remainder_y
      - .offset:         246
        .size:           2
        .value_kind:     hidden_remainder_z
      - .offset:         264
        .size:           8
        .value_kind:     hidden_global_offset_x
      - .offset:         272
        .size:           8
        .value_kind:     hidden_global_offset_y
      - .offset:         280
        .size:           8
        .value_kind:     hidden_global_offset_z
      - .offset:         288
        .size:           2
        .value_kind:     hidden_grid_dims
      - .offset:         344
        .size:           4
        .value_kind:     hidden_dynamic_lds_size
    .group_segment_fixed_size: 0
    .kernarg_segment_align: 8
    .kernarg_segment_size: 480
    .language:       OpenCL C
    .language_version:
      - 2
      - 0
    .max_flat_workgroup_size: 512
    .name:           _Z7enc_fwd4Args
    .private_segment_fixed_size: 0
    .sgpr_count:     108
    .sgpr_spill_count: 136
    .symbol:         _Z7enc_fwd4Args.kd
    .uniform_work_group_size: 1
    .uses_dynamic_stack: false
    .vgpr_count:     256
    .vgpr_spill_count: 0
    .wavefront_size: 64
